# hand-pipelined output-projection epilogue (row groups prefetched 3-4 deep, g loaded once per unit) + dn gate prefetch + XCD-aware dn deal
# speedup vs baseline: 1.0041x; 1.0041x over previous
.LBB0_872:
	s_lshl_b32 s4, s38, 8
	s_add_i32 s4, s4, s62
	v_or_b32_e32 v158, s4, v1
	v_lshl_or_b32 v159, s6, 8, v167
	s_lshr_b32 s5, s4, 11
	s_cmp_lt_u32 s4, 0x2000
	s_cselect_b32 s5, s5, 4
	s_cselect_b32 s7, 0, 0x2000
	s_cselect_b32 s16, 0, 16
	s_mul_i32 s5, s5, 0xc000
	s_add_u32 s28, s46, s5
	s_addc_u32 s29, s47, 0
	s_add_u32 s28, s28, s74
	s_addc_u32 s29, s29, s75
	v_lshlrev_b32_e32 v169, 2, v159
	global_load_dwordx2 v[178:179], v169, s[28:29]
	global_load_dwordx2 v[198:199], v169, s[28:29] offset:8
	global_load_dwordx2 v[220:221], v169, s[28:29] offset:16
	global_load_dwordx2 v[228:229], v169, s[28:29] offset:24
	global_load_dwordx2 v[232:233], v169, s[28:29] offset:512
	global_load_dwordx2 v[236:237], v169, s[28:29] offset:520
	global_load_dwordx2 v[164:165], v169, s[28:29] offset:528
	global_load_dwordx2 v[156:157], v169, s[28:29] offset:536
	v_subrev_u32_e32 v180, s7, v158
	v_lshlrev_b32_e32 v180, 13, v180
	v_lshlrev_b32_e32 v158, 12, v158
	v_lshl_add_u32 v158, v159, 1, v158
	v_lshl_add_u32 v159, v159, 2, v180
	v_readlane_b32 s38, v255, 0
	v_readlane_b32 s39, v255, 1
	s_add_u32 s40, s0, s16
	s_addc_u32 s41, s1, 0
	s_load_dwordx2 s[40:41], s[40:41], 0x0
	s_and_b64 vcc, exec, s[38:39]
	s_waitcnt lgkmcnt(0)
	s_cbranch_vccnz .Lepo_l1
	v_add_u32_e32 v180, 0x0, v159
	global_load_dwordx4 v[132:135], v180, s[40:41] offset:0
	global_load_dwordx4 v[136:139], v180, s[40:41] offset:16
	global_load_dwordx4 v[160:163], v180, s[40:41] offset:512
	global_load_dwordx4 v[170:173], v180, s[40:41] offset:528
	v_add_u32_e32 v180, 0x20000, v159
	global_load_dwordx4 v[174:177], v180, s[40:41] offset:0
	global_load_dwordx4 v[200:203], v180, s[40:41] offset:16
	global_load_dwordx4 v[204:207], v180, s[40:41] offset:512
	global_load_dwordx4 v[208:211], v180, s[40:41] offset:528
	v_add_u32_e32 v180, 0x40000, v159
	global_load_dwordx4 v[212:215], v180, s[40:41] offset:0
	global_load_dwordx4 v[216:219], v180, s[40:41] offset:16
	global_load_dwordx4 v[240:243], v180, s[40:41] offset:512
	global_load_dwordx4 v[246:249], v180, s[40:41] offset:528
	s_waitcnt vmcnt(8)
	v_add_u32_e32 v183, 0x0, v158
	v_pk_fma_f32 v[130:131], v[130:131], v[198:199], v[134:135]
	v_pk_fma_f32 v[128:129], v[128:129], v[178:179], v[132:133]
	v_pk_fma_f32 v[126:127], v[126:127], v[228:229], v[138:139]
	v_pk_fma_f32 v[124:125], v[124:125], v[220:221], v[136:137]
	v_cvt_pk_bf16_f32 v128, v128, v129
	v_cvt_pk_bf16_f32 v129, v130, v131
	v_cvt_pk_bf16_f32 v130, v124, v125
	v_cvt_pk_bf16_f32 v131, v126, v127
	global_store_dwordx4 v183, v[128:131], s[26:27]
	v_pk_fma_f32 v[122:123], v[122:123], v[236:237], v[162:163]
	v_pk_fma_f32 v[120:121], v[120:121], v[232:233], v[160:161]
	v_pk_fma_f32 v[118:119], v[118:119], v[156:157], v[172:173]
	v_pk_fma_f32 v[116:117], v[116:117], v[164:165], v[170:171]
	v_cvt_pk_bf16_f32 v120, v120, v121
	v_cvt_pk_bf16_f32 v121, v122, v123
	v_cvt_pk_bf16_f32 v122, v116, v117
	v_cvt_pk_bf16_f32 v123, v118, v119
	global_store_dwordx4 v183, v[120:123], s[26:27] offset:256
	s_nop 0
	v_add_u32_e32 v180, 0x60000, v159
	global_load_dwordx4 v[132:135], v180, s[40:41] offset:0
	global_load_dwordx4 v[136:139], v180, s[40:41] offset:16
	global_load_dwordx4 v[160:163], v180, s[40:41] offset:512
	global_load_dwordx4 v[170:173], v180, s[40:41] offset:528
	s_waitcnt vmcnt(10)
	v_add_u32_e32 v183, 0x10000, v158
	v_pk_fma_f32 v[114:115], v[114:115], v[198:199], v[176:177]
	v_pk_fma_f32 v[112:113], v[112:113], v[178:179], v[174:175]
	v_pk_fma_f32 v[110:111], v[110:111], v[228:229], v[202:203]
	v_pk_fma_f32 v[108:109], v[108:109], v[220:221], v[200:201]
	v_cvt_pk_bf16_f32 v112, v112, v113
	v_cvt_pk_bf16_f32 v113, v114, v115
	v_cvt_pk_bf16_f32 v114, v108, v109
	v_cvt_pk_bf16_f32 v115, v110, v111
	global_store_dwordx4 v183, v[112:115], s[26:27]
	v_pk_fma_f32 v[106:107], v[106:107], v[236:237], v[206:207]
	v_pk_fma_f32 v[104:105], v[104:105], v[232:233], v[204:205]
	v_pk_fma_f32 v[102:103], v[102:103], v[156:157], v[210:211]
	v_pk_fma_f32 v[100:101], v[100:101], v[164:165], v[208:209]
	v_cvt_pk_bf16_f32 v104, v104, v105
	v_cvt_pk_bf16_f32 v105, v106, v107
	v_cvt_pk_bf16_f32 v106, v100, v101
	v_cvt_pk_bf16_f32 v107, v102, v103
	global_store_dwordx4 v183, v[104:107], s[26:27] offset:256
	s_nop 0
	v_add_u32_e32 v180, 0x100000, v159
	global_load_dwordx4 v[174:177], v180, s[40:41] offset:0
	global_load_dwordx4 v[200:203], v180, s[40:41] offset:16
	global_load_dwordx4 v[204:207], v180, s[40:41] offset:512
	global_load_dwordx4 v[208:211], v180, s[40:41] offset:528
	s_waitcnt vmcnt(12)
	v_add_u32_e32 v183, 0x20000, v158
	v_pk_fma_f32 v[98:99], v[98:99], v[198:199], v[214:215]
	v_pk_fma_f32 v[96:97], v[96:97], v[178:179], v[212:213]
	v_pk_fma_f32 v[94:95], v[94:95], v[228:229], v[218:219]
	v_pk_fma_f32 v[92:93], v[92:93], v[220:221], v[216:217]
	v_cvt_pk_bf16_f32 v96, v96, v97
	v_cvt_pk_bf16_f32 v97, v98, v99
	v_cvt_pk_bf16_f32 v98, v92, v93
	v_cvt_pk_bf16_f32 v99, v94, v95
	global_store_dwordx4 v183, v[96:99], s[26:27]
	v_pk_fma_f32 v[90:91], v[90:91], v[236:237], v[242:243]
	v_pk_fma_f32 v[88:89], v[88:89], v[232:233], v[240:241]
	v_pk_fma_f32 v[86:87], v[86:87], v[156:157], v[248:249]
	v_pk_fma_f32 v[84:85], v[84:85], v[164:165], v[246:247]
	v_cvt_pk_bf16_f32 v88, v88, v89
	v_cvt_pk_bf16_f32 v89, v90, v91
	v_cvt_pk_bf16_f32 v90, v84, v85
	v_cvt_pk_bf16_f32 v91, v86, v87
	global_store_dwordx4 v183, v[88:91], s[26:27] offset:256
	s_nop 0
	v_add_u32_e32 v180, 0x120000, v159
	global_load_dwordx4 v[212:215], v180, s[40:41] offset:0
	global_load_dwordx4 v[216:219], v180, s[40:41] offset:16
	global_load_dwordx4 v[240:243], v180, s[40:41] offset:512
	global_load_dwordx4 v[246:249], v180, s[40:41] offset:528
	s_waitcnt vmcnt(12)
	v_add_u32_e32 v183, 0x30000, v158
	v_pk_fma_f32 v[82:83], v[82:83], v[198:199], v[134:135]
	v_pk_fma_f32 v[80:81], v[80:81], v[178:179], v[132:133]
	v_pk_fma_f32 v[78:79], v[78:79], v[228:229], v[138:139]
	v_pk_fma_f32 v[76:77], v[76:77], v[220:221], v[136:137]
	v_cvt_pk_bf16_f32 v80, v80, v81
	v_cvt_pk_bf16_f32 v81, v82, v83
	v_cvt_pk_bf16_f32 v82, v76, v77
	v_cvt_pk_bf16_f32 v83, v78, v79
	global_store_dwordx4 v183, v[80:83], s[26:27]
	v_pk_fma_f32 v[74:75], v[74:75], v[236:237], v[162:163]
	v_pk_fma_f32 v[72:73], v[72:73], v[232:233], v[160:161]
	v_pk_fma_f32 v[70:71], v[70:71], v[156:157], v[172:173]
	v_pk_fma_f32 v[68:69], v[68:69], v[164:165], v[170:171]
	v_cvt_pk_bf16_f32 v72, v72, v73
	v_cvt_pk_bf16_f32 v73, v74, v75
	v_cvt_pk_bf16_f32 v74, v68, v69
	v_cvt_pk_bf16_f32 v75, v70, v71
	global_store_dwordx4 v183, v[72:75], s[26:27] offset:256
	s_nop 0
	v_add_u32_e32 v180, 0x140000, v159
	global_load_dwordx4 v[132:135], v180, s[40:41] offset:0
	global_load_dwordx4 v[136:139], v180, s[40:41] offset:16
	global_load_dwordx4 v[160:163], v180, s[40:41] offset:512
	global_load_dwordx4 v[170:173], v180, s[40:41] offset:528
	s_waitcnt vmcnt(12)
	v_add_u32_e32 v183, 0x80000, v158
	v_pk_fma_f32 v[66:67], v[66:67], v[198:199], v[176:177]
	v_pk_fma_f32 v[64:65], v[64:65], v[178:179], v[174:175]
	v_pk_fma_f32 v[62:63], v[62:63], v[228:229], v[202:203]
	v_pk_fma_f32 v[60:61], v[60:61], v[220:221], v[200:201]
	v_cvt_pk_bf16_f32 v64, v64, v65
	v_cvt_pk_bf16_f32 v65, v66, v67
	v_cvt_pk_bf16_f32 v66, v60, v61
	v_cvt_pk_bf16_f32 v67, v62, v63
	global_store_dwordx4 v183, v[64:67], s[26:27]
	v_pk_fma_f32 v[58:59], v[58:59], v[236:237], v[206:207]
	v_pk_fma_f32 v[56:57], v[56:57], v[232:233], v[204:205]
	v_pk_fma_f32 v[54:55], v[54:55], v[156:157], v[210:211]
	v_pk_fma_f32 v[52:53], v[52:53], v[164:165], v[208:209]
	v_cvt_pk_bf16_f32 v56, v56, v57
	v_cvt_pk_bf16_f32 v57, v58, v59
	v_cvt_pk_bf16_f32 v58, v52, v53
	v_cvt_pk_bf16_f32 v59, v54, v55
	global_store_dwordx4 v183, v[56:59], s[26:27] offset:256
	s_nop 0
	v_add_u32_e32 v180, 0x160000, v159
	global_load_dwordx4 v[174:177], v180, s[40:41] offset:0
	global_load_dwordx4 v[200:203], v180, s[40:41] offset:16
	global_load_dwordx4 v[204:207], v180, s[40:41] offset:512
	global_load_dwordx4 v[208:211], v180, s[40:41] offset:528
	s_waitcnt vmcnt(12)
	v_add_u32_e32 v183, 0x90000, v158
	v_pk_fma_f32 v[50:51], v[50:51], v[198:199], v[214:215]
	v_pk_fma_f32 v[48:49], v[48:49], v[178:179], v[212:213]
	v_pk_fma_f32 v[46:47], v[46:47], v[228:229], v[218:219]
	v_pk_fma_f32 v[44:45], v[44:45], v[220:221], v[216:217]
	v_cvt_pk_bf16_f32 v48, v48, v49
	v_cvt_pk_bf16_f32 v49, v50, v51
	v_cvt_pk_bf16_f32 v50, v44, v45
	v_cvt_pk_bf16_f32 v51, v46, v47
	global_store_dwordx4 v183, v[48:51], s[26:27]
	v_pk_fma_f32 v[42:43], v[42:43], v[236:237], v[242:243]
	v_pk_fma_f32 v[40:41], v[40:41], v[232:233], v[240:241]
	v_pk_fma_f32 v[38:39], v[38:39], v[156:157], v[248:249]
	v_pk_fma_f32 v[36:37], v[36:37], v[164:165], v[246:247]
	v_cvt_pk_bf16_f32 v40, v40, v41
	v_cvt_pk_bf16_f32 v41, v42, v43
	v_cvt_pk_bf16_f32 v42, v36, v37
	v_cvt_pk_bf16_f32 v43, v38, v39
	global_store_dwordx4 v183, v[40:43], s[26:27] offset:256
	s_waitcnt vmcnt(8)
	v_add_u32_e32 v183, 0xa0000, v158
	v_pk_fma_f32 v[34:35], v[34:35], v[198:199], v[134:135]
	v_pk_fma_f32 v[32:33], v[32:33], v[178:179], v[132:133]
	v_pk_fma_f32 v[30:31], v[30:31], v[228:229], v[138:139]
	v_pk_fma_f32 v[28:29], v[28:29], v[220:221], v[136:137]
	v_cvt_pk_bf16_f32 v32, v32, v33
	v_cvt_pk_bf16_f32 v33, v34, v35
	v_cvt_pk_bf16_f32 v34, v28, v29
	v_cvt_pk_bf16_f32 v35, v30, v31
	global_store_dwordx4 v183, v[32:35], s[26:27]
	v_pk_fma_f32 v[26:27], v[26:27], v[236:237], v[162:163]
	v_pk_fma_f32 v[24:25], v[24:25], v[232:233], v[160:161]
	v_pk_fma_f32 v[22:23], v[22:23], v[156:157], v[172:173]
	v_pk_fma_f32 v[20:21], v[20:21], v[164:165], v[170:171]
	v_cvt_pk_bf16_f32 v24, v24, v25
	v_cvt_pk_bf16_f32 v25, v26, v27
	v_cvt_pk_bf16_f32 v26, v20, v21
	v_cvt_pk_bf16_f32 v27, v22, v23
	global_store_dwordx4 v183, v[24:27], s[26:27] offset:256
	s_waitcnt vmcnt(4)
	v_add_u32_e32 v183, 0xb0000, v158
	v_pk_fma_f32 v[18:19], v[18:19], v[198:199], v[176:177]
	v_pk_fma_f32 v[16:17], v[16:17], v[178:179], v[174:175]
	v_pk_fma_f32 v[14:15], v[14:15], v[228:229], v[202:203]
	v_pk_fma_f32 v[12:13], v[12:13], v[220:221], v[200:201]
	v_cvt_pk_bf16_f32 v16, v16, v17
	v_cvt_pk_bf16_f32 v17, v18, v19
	v_cvt_pk_bf16_f32 v18, v12, v13
	v_cvt_pk_bf16_f32 v19, v14, v15
	global_store_dwordx4 v183, v[16:19], s[26:27]
	v_pk_fma_f32 v[10:11], v[10:11], v[236:237], v[206:207]
	v_pk_fma_f32 v[8:9], v[8:9], v[232:233], v[204:205]
	v_pk_fma_f32 v[6:7], v[6:7], v[156:157], v[210:211]
	v_pk_fma_f32 v[4:5], v[4:5], v[164:165], v[208:209]
	v_cvt_pk_bf16_f32 v8, v8, v9
	v_cvt_pk_bf16_f32 v9, v10, v11
	v_cvt_pk_bf16_f32 v10, v4, v5
	v_cvt_pk_bf16_f32 v11, v6, v7
	global_store_dwordx4 v183, v[8:11], s[26:27] offset:256
	s_branch .Lepo_done
.Lepo_l1:
	v_add_u32_e32 v180, 0x0, v158
	global_load_dwordx4 v[132:135], v180, s[26:27]
	global_load_dwordx4 v[136:139], v180, s[26:27] offset:256
	v_add_u32_e32 v180, 0x10000, v158
	global_load_dwordx4 v[160:163], v180, s[26:27]
	global_load_dwordx4 v[170:173], v180, s[26:27] offset:256
	v_add_u32_e32 v180, 0x20000, v158
	global_load_dwordx4 v[174:177], v180, s[26:27]
	global_load_dwordx4 v[200:203], v180, s[26:27] offset:256
	v_add_u32_e32 v180, 0x30000, v158
	global_load_dwordx4 v[204:207], v180, s[26:27]
	global_load_dwordx4 v[208:211], v180, s[26:27] offset:256
	s_waitcnt vmcnt(6)
	v_add_u32_e32 v183, 0x0, v158
	v_lshlrev_b32_e32 v212, 16, v132
	v_and_b32_e32 v213, 0xffff0000, v132
	v_lshlrev_b32_e32 v214, 16, v133
	v_and_b32_e32 v215, 0xffff0000, v133
	v_lshlrev_b32_e32 v132, 16, v134
	v_and_b32_e32 v133, 0xffff0000, v134
	v_lshlrev_b32_e32 v134, 16, v135
	v_and_b32_e32 v135, 0xffff0000, v135
	v_pk_fma_f32 v[130:131], v[130:131], v[198:199], v[214:215]
	v_pk_fma_f32 v[128:129], v[128:129], v[178:179], v[212:213]
	v_pk_fma_f32 v[126:127], v[126:127], v[228:229], v[134:135]
	v_pk_fma_f32 v[124:125], v[124:125], v[220:221], v[132:133]
	v_cvt_pk_bf16_f32 v128, v128, v129
	v_cvt_pk_bf16_f32 v129, v130, v131
	v_cvt_pk_bf16_f32 v130, v124, v125
	v_cvt_pk_bf16_f32 v131, v126, v127
	global_store_dwordx4 v183, v[128:131], s[26:27]
	v_lshlrev_b32_e32 v212, 16, v136
	v_and_b32_e32 v213, 0xffff0000, v136
	v_lshlrev_b32_e32 v214, 16, v137
	v_and_b32_e32 v215, 0xffff0000, v137
	v_lshlrev_b32_e32 v136, 16, v138
	v_and_b32_e32 v137, 0xffff0000, v138
	v_lshlrev_b32_e32 v138, 16, v139
	v_and_b32_e32 v139, 0xffff0000, v139
	v_pk_fma_f32 v[122:123], v[122:123], v[236:237], v[214:215]
	v_pk_fma_f32 v[120:121], v[120:121], v[232:233], v[212:213]
	v_pk_fma_f32 v[118:119], v[118:119], v[156:157], v[138:139]
	v_pk_fma_f32 v[116:117], v[116:117], v[164:165], v[136:137]
	v_cvt_pk_bf16_f32 v120, v120, v121
	v_cvt_pk_bf16_f32 v121, v122, v123
	v_cvt_pk_bf16_f32 v122, v116, v117
	v_cvt_pk_bf16_f32 v123, v118, v119
	global_store_dwordx4 v183, v[120:123], s[26:27] offset:256
	s_nop 0
	v_add_u32_e32 v180, 0x80000, v158
	global_load_dwordx4 v[132:135], v180, s[26:27]
	global_load_dwordx4 v[136:139], v180, s[26:27] offset:256
	s_waitcnt vmcnt(8)
	v_add_u32_e32 v183, 0x10000, v158
	v_lshlrev_b32_e32 v212, 16, v160
	v_and_b32_e32 v213, 0xffff0000, v160
	v_lshlrev_b32_e32 v214, 16, v161
	v_and_b32_e32 v215, 0xffff0000, v161
	v_lshlrev_b32_e32 v160, 16, v162
	v_and_b32_e32 v161, 0xffff0000, v162
	v_lshlrev_b32_e32 v162, 16, v163
	v_and_b32_e32 v163, 0xffff0000, v163
	v_pk_fma_f32 v[114:115], v[114:115], v[198:199], v[214:215]
	v_pk_fma_f32 v[112:113], v[112:113], v[178:179], v[212:213]
	v_pk_fma_f32 v[110:111], v[110:111], v[228:229], v[162:163]
	v_pk_fma_f32 v[108:109], v[108:109], v[220:221], v[160:161]
	v_cvt_pk_bf16_f32 v112, v112, v113
	v_cvt_pk_bf16_f32 v113, v114, v115
	v_cvt_pk_bf16_f32 v114, v108, v109
	v_cvt_pk_bf16_f32 v115, v110, v111
	global_store_dwordx4 v183, v[112:115], s[26:27]
	v_lshlrev_b32_e32 v212, 16, v170
	v_and_b32_e32 v213, 0xffff0000, v170
	v_lshlrev_b32_e32 v214, 16, v171
	v_and_b32_e32 v215, 0xffff0000, v171
	v_lshlrev_b32_e32 v170, 16, v172
	v_and_b32_e32 v171, 0xffff0000, v172
	v_lshlrev_b32_e32 v172, 16, v173
	v_and_b32_e32 v173, 0xffff0000, v173
	v_pk_fma_f32 v[106:107], v[106:107], v[236:237], v[214:215]
	v_pk_fma_f32 v[104:105], v[104:105], v[232:233], v[212:213]
	v_pk_fma_f32 v[102:103], v[102:103], v[156:157], v[172:173]
	v_pk_fma_f32 v[100:101], v[100:101], v[164:165], v[170:171]
	v_cvt_pk_bf16_f32 v104, v104, v105
	v_cvt_pk_bf16_f32 v105, v106, v107
	v_cvt_pk_bf16_f32 v106, v100, v101
	v_cvt_pk_bf16_f32 v107, v102, v103
	global_store_dwordx4 v183, v[104:107], s[26:27] offset:256
	s_nop 0
	v_add_u32_e32 v180, 0x90000, v158
	global_load_dwordx4 v[160:163], v180, s[26:27]
	global_load_dwordx4 v[170:173], v180, s[26:27] offset:256
	s_waitcnt vmcnt(10)
	v_add_u32_e32 v183, 0x20000, v158
	v_lshlrev_b32_e32 v212, 16, v174
	v_and_b32_e32 v213, 0xffff0000, v174
	v_lshlrev_b32_e32 v214, 16, v175
	v_and_b32_e32 v215, 0xffff0000, v175
	v_lshlrev_b32_e32 v174, 16, v176
	v_and_b32_e32 v175, 0xffff0000, v176
	v_lshlrev_b32_e32 v176, 16, v177
	v_and_b32_e32 v177, 0xffff0000, v177
	v_pk_fma_f32 v[98:99], v[98:99], v[198:199], v[214:215]
	v_pk_fma_f32 v[96:97], v[96:97], v[178:179], v[212:213]
	v_pk_fma_f32 v[94:95], v[94:95], v[228:229], v[176:177]
	v_pk_fma_f32 v[92:93], v[92:93], v[220:221], v[174:175]
	v_cvt_pk_bf16_f32 v96, v96, v97
	v_cvt_pk_bf16_f32 v97, v98, v99
	v_cvt_pk_bf16_f32 v98, v92, v93
	v_cvt_pk_bf16_f32 v99, v94, v95
	global_store_dwordx4 v183, v[96:99], s[26:27]
	v_lshlrev_b32_e32 v212, 16, v200
	v_and_b32_e32 v213, 0xffff0000, v200
	v_lshlrev_b32_e32 v214, 16, v201
	v_and_b32_e32 v215, 0xffff0000, v201
	v_lshlrev_b32_e32 v200, 16, v202
	v_and_b32_e32 v201, 0xffff0000, v202
	v_lshlrev_b32_e32 v202, 16, v203
	v_and_b32_e32 v203, 0xffff0000, v203
	v_pk_fma_f32 v[90:91], v[90:91], v[236:237], v[214:215]
	v_pk_fma_f32 v[88:89], v[88:89], v[232:233], v[212:213]
	v_pk_fma_f32 v[86:87], v[86:87], v[156:157], v[202:203]
	v_pk_fma_f32 v[84:85], v[84:85], v[164:165], v[200:201]
	v_cvt_pk_bf16_f32 v88, v88, v89
	v_cvt_pk_bf16_f32 v89, v90, v91
	v_cvt_pk_bf16_f32 v90, v84, v85
	v_cvt_pk_bf16_f32 v91, v86, v87
	global_store_dwordx4 v183, v[88:91], s[26:27] offset:256
	s_nop 0
	v_add_u32_e32 v180, 0xa0000, v158
	global_load_dwordx4 v[174:177], v180, s[26:27]
	global_load_dwordx4 v[200:203], v180, s[26:27] offset:256
	s_waitcnt vmcnt(12)
	v_add_u32_e32 v183, 0x30000, v158
	v_lshlrev_b32_e32 v212, 16, v204
	v_and_b32_e32 v213, 0xffff0000, v204
	v_lshlrev_b32_e32 v214, 16, v205
	v_and_b32_e32 v215, 0xffff0000, v205
	v_lshlrev_b32_e32 v204, 16, v206
	v_and_b32_e32 v205, 0xffff0000, v206
	v_lshlrev_b32_e32 v206, 16, v207
	v_and_b32_e32 v207, 0xffff0000, v207
	v_pk_fma_f32 v[82:83], v[82:83], v[198:199], v[214:215]
	v_pk_fma_f32 v[80:81], v[80:81], v[178:179], v[212:213]
	v_pk_fma_f32 v[78:79], v[78:79], v[228:229], v[206:207]
	v_pk_fma_f32 v[76:77], v[76:77], v[220:221], v[204:205]
	v_cvt_pk_bf16_f32 v80, v80, v81
	v_cvt_pk_bf16_f32 v81, v82, v83
	v_cvt_pk_bf16_f32 v82, v76, v77
	v_cvt_pk_bf16_f32 v83, v78, v79
	global_store_dwordx4 v183, v[80:83], s[26:27]
	v_lshlrev_b32_e32 v212, 16, v208
	v_and_b32_e32 v213, 0xffff0000, v208
	v_lshlrev_b32_e32 v214, 16, v209
	v_and_b32_e32 v215, 0xffff0000, v209
	v_lshlrev_b32_e32 v208, 16, v210
	v_and_b32_e32 v209, 0xffff0000, v210
	v_lshlrev_b32_e32 v210, 16, v211
	v_and_b32_e32 v211, 0xffff0000, v211
	v_pk_fma_f32 v[74:75], v[74:75], v[236:237], v[214:215]
	v_pk_fma_f32 v[72:73], v[72:73], v[232:233], v[212:213]
	v_pk_fma_f32 v[70:71], v[70:71], v[156:157], v[210:211]
	v_pk_fma_f32 v[68:69], v[68:69], v[164:165], v[208:209]
	v_cvt_pk_bf16_f32 v72, v72, v73
	v_cvt_pk_bf16_f32 v73, v74, v75
	v_cvt_pk_bf16_f32 v74, v68, v69
	v_cvt_pk_bf16_f32 v75, v70, v71
	global_store_dwordx4 v183, v[72:75], s[26:27] offset:256
	s_nop 0
	v_add_u32_e32 v180, 0xb0000, v158
	global_load_dwordx4 v[204:207], v180, s[26:27]
	global_load_dwordx4 v[208:211], v180, s[26:27] offset:256
	s_waitcnt vmcnt(12)
	v_add_u32_e32 v183, 0x80000, v158
	v_lshlrev_b32_e32 v212, 16, v132
	v_and_b32_e32 v213, 0xffff0000, v132
	v_lshlrev_b32_e32 v214, 16, v133
	v_and_b32_e32 v215, 0xffff0000, v133
	v_lshlrev_b32_e32 v132, 16, v134
	v_and_b32_e32 v133, 0xffff0000, v134
	v_lshlrev_b32_e32 v134, 16, v135
	v_and_b32_e32 v135, 0xffff0000, v135
	v_pk_fma_f32 v[66:67], v[66:67], v[198:199], v[214:215]
	v_pk_fma_f32 v[64:65], v[64:65], v[178:179], v[212:213]
	v_pk_fma_f32 v[62:63], v[62:63], v[228:229], v[134:135]
	v_pk_fma_f32 v[60:61], v[60:61], v[220:221], v[132:133]
	v_cvt_pk_bf16_f32 v64, v64, v65
	v_cvt_pk_bf16_f32 v65, v66, v67
	v_cvt_pk_bf16_f32 v66, v60, v61
	v_cvt_pk_bf16_f32 v67, v62, v63
	global_store_dwordx4 v183, v[64:67], s[26:27]
	v_lshlrev_b32_e32 v212, 16, v136
	v_and_b32_e32 v213, 0xffff0000, v136
	v_lshlrev_b32_e32 v214, 16, v137
	v_and_b32_e32 v215, 0xffff0000, v137
	v_lshlrev_b32_e32 v136, 16, v138
	v_and_b32_e32 v137, 0xffff0000, v138
	v_lshlrev_b32_e32 v138, 16, v139
	v_and_b32_e32 v139, 0xffff0000, v139
	v_pk_fma_f32 v[58:59], v[58:59], v[236:237], v[214:215]
	v_pk_fma_f32 v[56:57], v[56:57], v[232:233], v[212:213]
	v_pk_fma_f32 v[54:55], v[54:55], v[156:157], v[138:139]
	v_pk_fma_f32 v[52:53], v[52:53], v[164:165], v[136:137]
	v_cvt_pk_bf16_f32 v56, v56, v57
	v_cvt_pk_bf16_f32 v57, v58, v59
	v_cvt_pk_bf16_f32 v58, v52, v53
	v_cvt_pk_bf16_f32 v59, v54, v55
	global_store_dwordx4 v183, v[56:59], s[26:27] offset:256
	s_waitcnt vmcnt(10)
	v_add_u32_e32 v183, 0x90000, v158
	v_lshlrev_b32_e32 v212, 16, v160
	v_and_b32_e32 v213, 0xffff0000, v160
	v_lshlrev_b32_e32 v214, 16, v161
	v_and_b32_e32 v215, 0xffff0000, v161
	v_lshlrev_b32_e32 v160, 16, v162
	v_and_b32_e32 v161, 0xffff0000, v162
	v_lshlrev_b32_e32 v162, 16, v163
	v_and_b32_e32 v163, 0xffff0000, v163
	v_pk_fma_f32 v[50:51], v[50:51], v[198:199], v[214:215]
	v_pk_fma_f32 v[48:49], v[48:49], v[178:179], v[212:213]
	v_pk_fma_f32 v[46:47], v[46:47], v[228:229], v[162:163]
	v_pk_fma_f32 v[44:45], v[44:45], v[220:221], v[160:161]
	v_cvt_pk_bf16_f32 v48, v48, v49
	v_cvt_pk_bf16_f32 v49, v50, v51
	v_cvt_pk_bf16_f32 v50, v44, v45
	v_cvt_pk_bf16_f32 v51, v46, v47
	global_store_dwordx4 v183, v[48:51], s[26:27]
	v_lshlrev_b32_e32 v212, 16, v170
	v_and_b32_e32 v213, 0xffff0000, v170
	v_lshlrev_b32_e32 v214, 16, v171
	v_and_b32_e32 v215, 0xffff0000, v171
	v_lshlrev_b32_e32 v170, 16, v172
	v_and_b32_e32 v171, 0xffff0000, v172
	v_lshlrev_b32_e32 v172, 16, v173
	v_and_b32_e32 v173, 0xffff0000, v173
	v_pk_fma_f32 v[42:43], v[42:43], v[236:237], v[214:215]
	v_pk_fma_f32 v[40:41], v[40:41], v[232:233], v[212:213]
	v_pk_fma_f32 v[38:39], v[38:39], v[156:157], v[172:173]
	v_pk_fma_f32 v[36:37], v[36:37], v[164:165], v[170:171]
	v_cvt_pk_bf16_f32 v40, v40, v41
	v_cvt_pk_bf16_f32 v41, v42, v43
	v_cvt_pk_bf16_f32 v42, v36, v37
	v_cvt_pk_bf16_f32 v43, v38, v39
	global_store_dwordx4 v183, v[40:43], s[26:27] offset:256
	s_waitcnt vmcnt(8)
	v_add_u32_e32 v183, 0xa0000, v158
	v_lshlrev_b32_e32 v212, 16, v174
	v_and_b32_e32 v213, 0xffff0000, v174
	v_lshlrev_b32_e32 v214, 16, v175
	v_and_b32_e32 v215, 0xffff0000, v175
	v_lshlrev_b32_e32 v174, 16, v176
	v_and_b32_e32 v175, 0xffff0000, v176
	v_lshlrev_b32_e32 v176, 16, v177
	v_and_b32_e32 v177, 0xffff0000, v177
	v_pk_fma_f32 v[34:35], v[34:35], v[198:199], v[214:215]
	v_pk_fma_f32 v[32:33], v[32:33], v[178:179], v[212:213]
	v_pk_fma_f32 v[30:31], v[30:31], v[228:229], v[176:177]
	v_pk_fma_f32 v[28:29], v[28:29], v[220:221], v[174:175]
	v_cvt_pk_bf16_f32 v32, v32, v33
	v_cvt_pk_bf16_f32 v33, v34, v35
	v_cvt_pk_bf16_f32 v34, v28, v29
	v_cvt_pk_bf16_f32 v35, v30, v31
	global_store_dwordx4 v183, v[32:35], s[26:27]
	v_lshlrev_b32_e32 v212, 16, v200
	v_and_b32_e32 v213, 0xffff0000, v200
	v_lshlrev_b32_e32 v214, 16, v201
	v_and_b32_e32 v215, 0xffff0000, v201
	v_lshlrev_b32_e32 v200, 16, v202
	v_and_b32_e32 v201, 0xffff0000, v202
	v_lshlrev_b32_e32 v202, 16, v203
	v_and_b32_e32 v203, 0xffff0000, v203
	v_pk_fma_f32 v[26:27], v[26:27], v[236:237], v[214:215]
	v_pk_fma_f32 v[24:25], v[24:25], v[232:233], v[212:213]
	v_pk_fma_f32 v[22:23], v[22:23], v[156:157], v[202:203]
	v_pk_fma_f32 v[20:21], v[20:21], v[164:165], v[200:201]
	v_cvt_pk_bf16_f32 v24, v24, v25
	v_cvt_pk_bf16_f32 v25, v26, v27
	v_cvt_pk_bf16_f32 v26, v20, v21
	v_cvt_pk_bf16_f32 v27, v22, v23
	global_store_dwordx4 v183, v[24:27], s[26:27] offset:256
	s_waitcnt vmcnt(6)
	v_add_u32_e32 v183, 0xb0000, v158
	v_lshlrev_b32_e32 v212, 16, v204
	v_and_b32_e32 v213, 0xffff0000, v204
	v_lshlrev_b32_e32 v214, 16, v205
	v_and_b32_e32 v215, 0xffff0000, v205
	v_lshlrev_b32_e32 v204, 16, v206
	v_and_b32_e32 v205, 0xffff0000, v206
	v_lshlrev_b32_e32 v206, 16, v207
	v_and_b32_e32 v207, 0xffff0000, v207
	v_pk_fma_f32 v[18:19], v[18:19], v[198:199], v[214:215]
	v_pk_fma_f32 v[16:17], v[16:17], v[178:179], v[212:213]
	v_pk_fma_f32 v[14:15], v[14:15], v[228:229], v[206:207]
	v_pk_fma_f32 v[12:13], v[12:13], v[220:221], v[204:205]
	v_cvt_pk_bf16_f32 v16, v16, v17
	v_cvt_pk_bf16_f32 v17, v18, v19
	v_cvt_pk_bf16_f32 v18, v12, v13
	v_cvt_pk_bf16_f32 v19, v14, v15
	global_store_dwordx4 v183, v[16:19], s[26:27]
	v_lshlrev_b32_e32 v212, 16, v208
	v_and_b32_e32 v213, 0xffff0000, v208
	v_lshlrev_b32_e32 v214, 16, v209
	v_and_b32_e32 v215, 0xffff0000, v209
	v_lshlrev_b32_e32 v208, 16, v210
	v_and_b32_e32 v209, 0xffff0000, v210
	v_lshlrev_b32_e32 v210, 16, v211
	v_and_b32_e32 v211, 0xffff0000, v211
	v_pk_fma_f32 v[10:11], v[10:11], v[236:237], v[214:215]
	v_pk_fma_f32 v[8:9], v[8:9], v[232:233], v[212:213]
	v_pk_fma_f32 v[6:7], v[6:7], v[156:157], v[210:211]
	v_pk_fma_f32 v[4:5], v[4:5], v[164:165], v[208:209]
	v_cvt_pk_bf16_f32 v8, v8, v9
	v_cvt_pk_bf16_f32 v9, v10, v11
	v_cvt_pk_bf16_f32 v10, v4, v5
	v_cvt_pk_bf16_f32 v11, v6, v7
	global_store_dwordx4 v183, v[8:11], s[26:27] offset:256
.Lepo_done:
	s_andn2_b64 vcc, exec, s[54:55]
	s_mov_b64 s[16:17], -1
	s_cbranch_vccnz .LBB0_865
	s_andn2_b64 vcc, exec, s[42:43]
	s_cbranch_vccnz .LBB0_864
	s_barrier
	s_branch .LBB0_864
